# grid barrier: acquire-side buffer_inv sc1 issued at arrival (non-leader: with first poll; XCD leader: with its wbl2) instead of after the release flag, 31 of 33 sites
# speedup vs baseline: 1.0131x; 1.0043x over previous
; __device__ __forceinline__ unsigned xb_ld(unsigned* p)              { return __hip_atomic_load(p, __ATOMIC_RELAXED, __HIP_MEMORY_SCOPE_AGENT); }
; __device__ __forceinline__ unsigned xb_add(unsigned* p, unsigned v) { return __hip_atomic_fetch_add(p, v, __ATOMIC_RELAXED, __HIP_MEMORY_SCOPE_AGENT); }
; #define XB_SPIN(cond, bar) do { unsigned _sp = 0; while (cond) { __builtin_amdgcn_s_sleep(1); \
;     if ((++_sp & 255u) == 0u) { if (xb_ld(&(bar)[XB_TMO])) break; if (_sp > XB_SPIN_CAP) { atomicAdd(&(bar)[XB_TMO], 1u); break; } } } } while (0)
; __device__ __forceinline__ void xcd_barrier(const XcdBarrier& b) {
;     ...
;         unsigned nloc = b.st[0], nx = b.st[1];
;         if (nloc == 0u) { xcd_barrier_complete(bar, b.x, nloc, nx); b.st[0] = nloc; b.st[1] = nx; }
;         const unsigned old = xb_add(&bar[XB_XSUB(b.x)], 1u);
;         const unsigned gen = old / nloc;
;         if (old + 1u == (gen + 1u) * nloc) {
;             __builtin_amdgcn_fence(__ATOMIC_RELEASE, "agent");
;             asm volatile("s_waitcnt vmcnt(0)" ::: "memory");
;             const unsigned og = xb_add(&bar[XB_TOP], 1u);
;             const unsigned tg = og / nx;
;             if (og + 1u == (tg + 1u) * nx) xb_add(&bar[XB_TOPGEN], 1u);
;             else XB_SPIN(xb_ld(&bar[XB_TOPGEN]) == tg, bar);
;             __builtin_amdgcn_fence(__ATOMIC_ACQUIRE, "agent");
;             xb_add(&bar[XB_XGEN(b.x)], 1u);
;             asm volatile("s_waitcnt vmcnt(0)" ::: "memory");
;         } else {
;             XB_SPIN(xb_ld(&bar[XB_XGEN(b.x)]) == gen, bar);
;             __builtin_amdgcn_fence(__ATOMIC_ACQUIRE, "agent");
;             asm volatile("s_waitcnt vmcnt(0)" ::: "memory");
.LBB0_65:
	v_readlane_b32 s2, v253, 6
	s_lshl_b32 s2, s2, 8
	v_readlane_b32 s4, v253, 4
	v_readlane_b32 s5, v253, 5
	s_add_u32 s2, s4, s2
	s_addc_u32 s3, s5, 0
	v_mov_b32_e32 v2, 0x1000
	v_mov_b32_e32 v4, 1
	global_atomic_add v4, v2, v4, s[2:3] offset:1024 sc0
	v_cvt_f32_u32_e32 v2, v3
	v_sub_u32_e32 v5, 0, v3
	v_rcp_iflag_f32_e32 v2, v2
	s_nop 0
	v_mul_f32_e32 v2, 0x4f7ffffe, v2
	v_cvt_u32_f32_e32 v2, v2
	v_mul_lo_u32 v5, v5, v2
	v_mul_hi_u32 v5, v2, v5
	v_add_u32_e32 v2, v2, v5
	s_waitcnt vmcnt(0)
	v_mul_hi_u32 v2, v4, v2
	v_mul_lo_u32 v5, v2, v3
	v_sub_u32_e32 v5, v4, v5
	v_add_u32_e32 v6, 1, v2
	v_cmp_ge_u32_e32 vcc, v5, v3
	v_add_u32_e32 v4, 1, v4
	s_nop 0
	v_cndmask_b32_e32 v2, v2, v6, vcc
	v_sub_u32_e32 v6, v5, v3
	v_cndmask_b32_e32 v5, v5, v6, vcc
	v_add_u32_e32 v6, 1, v2
	v_cmp_ge_u32_e32 vcc, v5, v3
	s_nop 1
	v_cndmask_b32_e32 v2, v2, v6, vcc
	v_mul_lo_u32 v5, v3, v2
	v_add_u32_e32 v3, v5, v3
	v_cmp_ne_u32_e32 vcc, v4, v3
	s_and_saveexec_b64 s[4:5], vcc
	s_xor_b64 s[4:5], exec, s[4:5]
	s_cbranch_execz .LBB0_79
	s_waitcnt lgkmcnt(0)
	buffer_inv sc1
	v_mov_b32_e32 v1, 0x2000
	global_load_dword v1, v1, s[2:3] offset:1024 sc1
	s_add_u32 s10, s2, 0x2400
	s_addc_u32 s11, s3, 0
	s_waitcnt vmcnt(0)
	v_cmp_eq_u32_e32 vcc, v1, v2
	s_and_saveexec_b64 s[6:7], vcc
	s_cbranch_execz .LBB0_78
	s_add_u32 s8, s94, 0x4200
	s_addc_u32 s9, s95, 0
	s_mov_b32 s22, 1
	s_mov_b64 s[12:13], 0
	v_mov_b32_e32 v1, 0
	s_branch .LBB0_69

; __device__ __forceinline__ unsigned xb_ld(unsigned* p)              { return __hip_atomic_load(p, __ATOMIC_RELAXED, __HIP_MEMORY_SCOPE_AGENT); }
; __device__ __forceinline__ unsigned xb_add(unsigned* p, unsigned v) { return __hip_atomic_fetch_add(p, v, __ATOMIC_RELAXED, __HIP_MEMORY_SCOPE_AGENT); }
; #define XB_SPIN(cond, bar) do { unsigned _sp = 0; while (cond) { __builtin_amdgcn_s_sleep(1); \
;     if ((++_sp & 255u) == 0u) { if (xb_ld(&(bar)[XB_TMO])) break; if (_sp > XB_SPIN_CAP) { atomicAdd(&(bar)[XB_TMO], 1u); break; } } } } while (0)
; __device__ __forceinline__ void xcd_barrier(const XcdBarrier& b) {
;     ...
;             __builtin_amdgcn_fence(__ATOMIC_RELEASE, "agent");
;             asm volatile("s_waitcnt vmcnt(0)" ::: "memory");
;             const unsigned og = xb_add(&bar[XB_TOP], 1u);
;             const unsigned tg = og / nx;
;             if (og + 1u == (tg + 1u) * nx) xb_add(&bar[XB_TOPGEN], 1u);
;             else XB_SPIN(xb_ld(&bar[XB_TOPGEN]) == tg, bar);
;             __builtin_amdgcn_fence(__ATOMIC_ACQUIRE, "agent");
;             xb_add(&bar[XB_XGEN(b.x)], 1u);
;             asm volatile("s_waitcnt vmcnt(0)" ::: "memory");
;         } else {
;             XB_SPIN(xb_ld(&bar[XB_XGEN(b.x)]) == gen, bar);
;             __builtin_amdgcn_fence(__ATOMIC_ACQUIRE, "agent");
;             asm volatile("s_waitcnt vmcnt(0)" ::: "memory");
;         }
.LBB0_78:
	s_or_b64 exec, exec, s[6:7]
	s_waitcnt vmcnt(0)
	s_waitcnt vmcnt(0)
.LBB0_79:
	s_andn2_saveexec_b64 s[4:5], s[4:5]
	s_cbranch_execz .LBB0_97
	s_mov_b64 s[4:5], exec
	buffer_wbl2 sc1
	buffer_inv sc1
	s_waitcnt lgkmcnt(0)
	s_waitcnt vmcnt(0)
	v_mbcnt_lo_u32_b32 v2, s4, 0
	v_mbcnt_hi_u32_b32 v2, s5, v2
	v_cmp_eq_u32_e32 vcc, 0, v2
	s_and_saveexec_b64 s[6:7], vcc
	s_cbranch_execz .LBB0_82
	s_bcnt1_i32_b64 s4, s[4:5]
	v_mov_b32_e32 v3, 0x7000
	v_mov_b32_e32 v4, s4
	global_atomic_add v3, v3, v4, s[94:95] offset:1024 sc0

; __device__ __forceinline__ unsigned xb_add(unsigned* p, unsigned v) { return __hip_atomic_fetch_add(p, v, __ATOMIC_RELAXED, __HIP_MEMORY_SCOPE_AGENT); }
; __device__ __forceinline__ void xcd_barrier(const XcdBarrier& b) {
;     ...
;             __builtin_amdgcn_fence(__ATOMIC_ACQUIRE, "agent");
;             xb_add(&bar[XB_XGEN(b.x)], 1u);
;             asm volatile("s_waitcnt vmcnt(0)" ::: "memory");
.LBB0_96:
	s_or_b64 exec, exec, s[4:5]
	v_mov_b32_e32 v1, 0x2000
	v_mov_b32_e32 v2, 1
	s_waitcnt vmcnt(0)
	global_atomic_add v1, v2, s[2:3] offset:1024
	s_waitcnt vmcnt(0)

; __device__ __forceinline__ unsigned xb_ld(unsigned* p)              { return __hip_atomic_load(p, __ATOMIC_RELAXED, __HIP_MEMORY_SCOPE_AGENT); }
; __device__ __forceinline__ unsigned xb_add(unsigned* p, unsigned v) { return __hip_atomic_fetch_add(p, v, __ATOMIC_RELAXED, __HIP_MEMORY_SCOPE_AGENT); }
; #define XB_SPIN(cond, bar) do { unsigned _sp = 0; while (cond) { __builtin_amdgcn_s_sleep(1); \
;     if ((++_sp & 255u) == 0u) { if (xb_ld(&(bar)[XB_TMO])) break; if (_sp > XB_SPIN_CAP) { atomicAdd(&(bar)[XB_TMO], 1u); break; } } } } while (0)
; __device__ __forceinline__ void xcd_barrier(const XcdBarrier& b) {
;     ...
;         unsigned nloc = b.st[0], nx = b.st[1];
;         if (nloc == 0u) { xcd_barrier_complete(bar, b.x, nloc, nx); b.st[0] = nloc; b.st[1] = nx; }
;         const unsigned old = xb_add(&bar[XB_XSUB(b.x)], 1u);
;         const unsigned gen = old / nloc;
;         if (old + 1u == (gen + 1u) * nloc) {
;             __builtin_amdgcn_fence(__ATOMIC_RELEASE, "agent");
;             asm volatile("s_waitcnt vmcnt(0)" ::: "memory");
;             const unsigned og = xb_add(&bar[XB_TOP], 1u);
;             const unsigned tg = og / nx;
;             if (og + 1u == (tg + 1u) * nx) xb_add(&bar[XB_TOPGEN], 1u);
;             else XB_SPIN(xb_ld(&bar[XB_TOPGEN]) == tg, bar);
;             __builtin_amdgcn_fence(__ATOMIC_ACQUIRE, "agent");
;             xb_add(&bar[XB_XGEN(b.x)], 1u);
;             asm volatile("s_waitcnt vmcnt(0)" ::: "memory");
;         } else {
;             XB_SPIN(xb_ld(&bar[XB_XGEN(b.x)]) == gen, bar);
;             __builtin_amdgcn_fence(__ATOMIC_ACQUIRE, "agent");
;             asm volatile("s_waitcnt vmcnt(0)" ::: "memory");
.LBB0_226:
	v_readlane_b32 s2, v253, 6
	s_lshl_b32 s2, s2, 8
	v_readlane_b32 s4, v253, 4
	v_readlane_b32 s5, v253, 5
	s_add_u32 s2, s4, s2
	s_addc_u32 s3, s5, 0
	v_mov_b32_e32 v3, 0x1000
	v_mov_b32_e32 v5, 1
	global_atomic_add v5, v3, v5, s[2:3] offset:1024 sc0
	v_cvt_f32_u32_e32 v3, v4
	v_sub_u32_e32 v6, 0, v4
	v_rcp_iflag_f32_e32 v3, v3
	s_nop 0
	v_mul_f32_e32 v3, 0x4f7ffffe, v3
	v_cvt_u32_f32_e32 v3, v3
	v_mul_lo_u32 v6, v6, v3
	v_mul_hi_u32 v6, v3, v6
	v_add_u32_e32 v3, v3, v6
	s_waitcnt vmcnt(0)
	v_mul_hi_u32 v3, v5, v3
	v_mul_lo_u32 v6, v3, v4
	v_sub_u32_e32 v6, v5, v6
	v_add_u32_e32 v7, 1, v3
	v_cmp_ge_u32_e32 vcc, v6, v4
	v_add_u32_e32 v5, 1, v5
	s_nop 0
	v_cndmask_b32_e32 v3, v3, v7, vcc
	v_sub_u32_e32 v7, v6, v4
	v_cndmask_b32_e32 v6, v6, v7, vcc
	v_add_u32_e32 v7, 1, v3
	v_cmp_ge_u32_e32 vcc, v6, v4
	s_nop 1
	v_cndmask_b32_e32 v3, v3, v7, vcc
	v_mul_lo_u32 v6, v4, v3
	v_add_u32_e32 v4, v6, v4
	v_cmp_ne_u32_e32 vcc, v5, v4
	s_and_saveexec_b64 s[4:5], vcc
	s_xor_b64 s[4:5], exec, s[4:5]
	s_cbranch_execz .LBB0_240
	s_waitcnt lgkmcnt(0)
	buffer_inv sc1
	v_mov_b32_e32 v2, 0x2000
	global_load_dword v2, v2, s[2:3] offset:1024 sc1
	s_add_u32 s10, s2, 0x2400
	s_addc_u32 s11, s3, 0
	s_waitcnt vmcnt(0)
	v_cmp_eq_u32_e32 vcc, v2, v3
	s_and_saveexec_b64 s[6:7], vcc
	s_cbranch_execz .LBB0_239
	s_add_u32 s8, s94, 0x4200
	s_addc_u32 s9, s95, 0
	s_mov_b32 s22, 1
	s_mov_b64 s[12:13], 0
	v_mov_b32_e32 v2, 0
	s_branch .LBB0_230

; __device__ __forceinline__ unsigned xb_add(unsigned* p, unsigned v) { return __hip_atomic_fetch_add(p, v, __ATOMIC_RELAXED, __HIP_MEMORY_SCOPE_AGENT); }
; __device__ __forceinline__ void xcd_barrier(const XcdBarrier& b) {
;     ...
;             __builtin_amdgcn_fence(__ATOMIC_RELEASE, "agent");
;             asm volatile("s_waitcnt vmcnt(0)" ::: "memory");
;             const unsigned og = xb_add(&bar[XB_TOP], 1u);
.LBB0_240:
	s_andn2_saveexec_b64 s[4:5], s[4:5]
	s_cbranch_execz .LBB0_258
	s_mov_b64 s[4:5], exec
	buffer_wbl2 sc1
	buffer_inv sc1
	s_waitcnt lgkmcnt(0)
	s_waitcnt vmcnt(0)
	v_mbcnt_lo_u32_b32 v3, s4, 0
	v_mbcnt_hi_u32_b32 v3, s5, v3
	v_cmp_eq_u32_e32 vcc, 0, v3
	s_and_saveexec_b64 s[6:7], vcc
	s_cbranch_execz .LBB0_243
	s_bcnt1_i32_b64 s4, s[4:5]
	v_mov_b32_e32 v4, 0x7000
	v_mov_b32_e32 v5, s4
	global_atomic_add v4, v4, v5, s[94:95] offset:1024 sc0

; __device__ __forceinline__ unsigned xb_add(unsigned* p, unsigned v) { return __hip_atomic_fetch_add(p, v, __ATOMIC_RELAXED, __HIP_MEMORY_SCOPE_AGENT); }
; __device__ __forceinline__ void xcd_barrier(const XcdBarrier& b) {
;     ...
;             __builtin_amdgcn_fence(__ATOMIC_ACQUIRE, "agent");
;             xb_add(&bar[XB_XGEN(b.x)], 1u);
;             asm volatile("s_waitcnt vmcnt(0)" ::: "memory");
.LBB0_257:
	s_or_b64 exec, exec, s[4:5]
	v_mov_b32_e32 v2, 0x2000
	v_mov_b32_e32 v3, 1
	s_waitcnt vmcnt(0)
	global_atomic_add v2, v3, s[2:3] offset:1024
	s_waitcnt vmcnt(0)

; __device__ __forceinline__ unsigned xb_ld(unsigned* p)              { return __hip_atomic_load(p, __ATOMIC_RELAXED, __HIP_MEMORY_SCOPE_AGENT); }
; __device__ __forceinline__ unsigned xb_add(unsigned* p, unsigned v) { return __hip_atomic_fetch_add(p, v, __ATOMIC_RELAXED, __HIP_MEMORY_SCOPE_AGENT); }
; #define XB_SPIN(cond, bar) do { unsigned _sp = 0; while (cond) { __builtin_amdgcn_s_sleep(1); \
;     if ((++_sp & 255u) == 0u) { if (xb_ld(&(bar)[XB_TMO])) break; if (_sp > XB_SPIN_CAP) { atomicAdd(&(bar)[XB_TMO], 1u); break; } } } } while (0)
; __device__ __forceinline__ void xcd_barrier(const XcdBarrier& b) {
;     ...
;         unsigned nloc = b.st[0], nx = b.st[1];
;         if (nloc == 0u) { xcd_barrier_complete(bar, b.x, nloc, nx); b.st[0] = nloc; b.st[1] = nx; }
;         const unsigned old = xb_add(&bar[XB_XSUB(b.x)], 1u);
;         const unsigned gen = old / nloc;
;         if (old + 1u == (gen + 1u) * nloc) {
;             __builtin_amdgcn_fence(__ATOMIC_RELEASE, "agent");
;             asm volatile("s_waitcnt vmcnt(0)" ::: "memory");
;             const unsigned og = xb_add(&bar[XB_TOP], 1u);
;             const unsigned tg = og / nx;
;             if (og + 1u == (tg + 1u) * nx) xb_add(&bar[XB_TOPGEN], 1u);
;             else XB_SPIN(xb_ld(&bar[XB_TOPGEN]) == tg, bar);
;             __builtin_amdgcn_fence(__ATOMIC_ACQUIRE, "agent");
;             xb_add(&bar[XB_XGEN(b.x)], 1u);
;             asm volatile("s_waitcnt vmcnt(0)" ::: "memory");
;         } else {
;             XB_SPIN(xb_ld(&bar[XB_XGEN(b.x)]) == gen, bar);
;             __builtin_amdgcn_fence(__ATOMIC_ACQUIRE, "agent");
;             asm volatile("s_waitcnt vmcnt(0)" ::: "memory");
.LBB0_4431:
	v_readlane_b32 s0, v253, 6
	s_lshl_b32 s0, s0, 8
	v_readlane_b32 s4, v253, 4
	v_readlane_b32 s5, v253, 5
	s_add_u32 s0, s4, s0
	s_addc_u32 s1, s5, 0
	v_mov_b32_e32 v2, 0x1000
	v_mov_b32_e32 v4, 1
	global_atomic_add v4, v2, v4, s[0:1] offset:1024 sc0
	v_cvt_f32_u32_e32 v2, v3
	v_sub_u32_e32 v5, 0, v3
	v_rcp_iflag_f32_e32 v2, v2
	s_nop 0
	v_mul_f32_e32 v2, 0x4f7ffffe, v2
	v_cvt_u32_f32_e32 v2, v2
	v_mul_lo_u32 v5, v5, v2
	v_mul_hi_u32 v5, v2, v5
	v_add_u32_e32 v2, v2, v5
	s_waitcnt vmcnt(0)
	v_mul_hi_u32 v2, v4, v2
	v_mul_lo_u32 v5, v2, v3
	v_sub_u32_e32 v5, v4, v5
	v_add_u32_e32 v6, 1, v2
	v_cmp_ge_u32_e32 vcc, v5, v3
	v_add_u32_e32 v4, 1, v4
	s_nop 0
	v_cndmask_b32_e32 v2, v2, v6, vcc
	v_sub_u32_e32 v6, v5, v3
	v_cndmask_b32_e32 v5, v5, v6, vcc
	v_add_u32_e32 v6, 1, v2
	v_cmp_ge_u32_e32 vcc, v5, v3
	s_nop 1
	v_cndmask_b32_e32 v2, v2, v6, vcc
	v_mul_lo_u32 v5, v3, v2
	v_add_u32_e32 v3, v5, v3
	v_cmp_ne_u32_e32 vcc, v4, v3
	s_and_saveexec_b64 s[4:5], vcc
	s_xor_b64 s[4:5], exec, s[4:5]
	s_cbranch_execz .LBB0_4445
	s_waitcnt lgkmcnt(0)
	buffer_inv sc1
	v_mov_b32_e32 v1, 0x2000
	global_load_dword v1, v1, s[0:1] offset:1024 sc1
	s_add_u32 s10, s0, 0x2400
	s_addc_u32 s11, s1, 0
	s_waitcnt vmcnt(0)
	v_cmp_eq_u32_e32 vcc, v1, v2
	s_and_saveexec_b64 s[6:7], vcc
	s_cbranch_execz .LBB0_4444
	s_add_u32 s8, s94, 0x4200
	s_addc_u32 s9, s95, 0
	s_mov_b32 s22, 1
	s_mov_b64 s[12:13], 0
	v_mov_b32_e32 v1, 0
	s_branch .LBB0_4435

; __device__ __forceinline__ unsigned xb_add(unsigned* p, unsigned v) { return __hip_atomic_fetch_add(p, v, __ATOMIC_RELAXED, __HIP_MEMORY_SCOPE_AGENT); }
; __device__ __forceinline__ void xcd_barrier(const XcdBarrier& b) {
;     ...
;             __builtin_amdgcn_fence(__ATOMIC_ACQUIRE, "agent");
;             xb_add(&bar[XB_XGEN(b.x)], 1u);
;             asm volatile("s_waitcnt vmcnt(0)" ::: "memory");
.LBB0_4462:
	s_or_b64 exec, exec, s[4:5]
	v_mov_b32_e32 v1, 0x2000
	v_mov_b32_e32 v2, 1
	s_waitcnt vmcnt(0)
	global_atomic_add v1, v2, s[0:1] offset:1024
	s_waitcnt vmcnt(0)
